# grid barrier: everyone waits on the top-level arrival counter itself (done at (generation+1) x leaders) instead of a generation word the last leader bumps after its arrival atomic returns
# speedup vs baseline: 1.0078x; 1.0030x over previous
.LBB0_69:
	s_or_b64 exec, exec, s[10:11]
	v_cvt_f32_u32_e32 v5, v3
	s_waitcnt vmcnt(0)
	v_readfirstlane_b32 s8, v4
	v_sub_u32_e32 v4, 0, v3
	v_rcp_iflag_f32_e32 v5, v5
	v_add_u32_e32 v6, s8, v2
	v_mul_f32_e32 v5, 0x4f7ffffe, v5
	v_cvt_u32_f32_e32 v5, v5
	v_mul_lo_u32 v2, v4, v5
	v_mul_hi_u32 v2, v5, v2
	v_add_u32_e32 v2, v5, v2
	v_mul_hi_u32 v2, v6, v2
	v_mul_lo_u32 v4, v2, v3
	v_sub_u32_e32 v4, v6, v4
	v_add_u32_e32 v5, 1, v2
	v_cmp_ge_u32_e32 vcc, v4, v3
	s_nop 1
	v_cndmask_b32_e32 v2, v2, v5, vcc
	v_sub_u32_e32 v5, v4, v3
	v_cndmask_b32_e32 v4, v4, v5, vcc
	v_add_u32_e32 v5, 1, v2
	v_cmp_ge_u32_e32 vcc, v4, v3
	v_add_u32_e32 v4, 1, v6
	s_nop 0
	v_cndmask_b32_e32 v2, v2, v5, vcc
	v_mul_lo_u32 v5, v3, v2
	v_add_u32_e32 v3, v5, v3
	v_cmp_ne_u32_e32 vcc, v4, v3
	s_and_saveexec_b64 s[8:9], vcc
	s_xor_b64 s[8:9], exec, s[8:9]
	s_cbranch_execz .LBB0_83
	s_waitcnt lgkmcnt(0)
	v_mad_u32_u24 v2, v1, v2, v1
	buffer_inv sc1
	v_mov_b32_e32 v1, 0xb000
	global_load_dword v1, v1, s[40:41] offset:1024 sc1
	s_add_u32 s22, s40, 0xb400
	s_addc_u32 s23, s41, 0
	s_waitcnt vmcnt(0)
	v_cmp_lt_u32_e32 vcc, v1, v2
	s_and_saveexec_b64 s[10:11], vcc
	s_cbranch_execz .LBB0_82
	s_add_u32 s20, s40, 0x8200
	s_addc_u32 s21, s41, 0
	s_mov_b32 s38, 1
	s_mov_b64 s[24:25], 0
	v_mov_b32_e32 v1, 0
	s_branch .LBB0_73

.LBB0_75:
	global_load_dword v3, v1, s[22:23] sc1
	s_add_i32 s38, s38, 1
	s_mov_b64 s[30:31], -1
	s_waitcnt vmcnt(0)
	v_cmp_ge_u32_e32 vcc, v3, v2
	s_orn2_b64 s[28:29], vcc, exec
	s_branch .LBB0_72

.LBB0_86:
	s_or_b64 exec, exec, s[10:11]
	v_cvt_f32_u32_e32 v4, v1
	s_waitcnt vmcnt(0)
	v_readfirstlane_b32 s8, v3
	s_add_u32 s10, s40, 0xb500
	s_addc_u32 s11, s41, 0
	v_rcp_iflag_f32_e32 v4, v4
	v_add_u32_e32 v2, s8, v2
	v_add_u32_e32 v5, 1, v2
	s_mov_b64 s[20:21], -1
	v_mul_f32_e32 v3, 0x4f7ffffe, v4
	v_cvt_u32_f32_e32 v3, v3
	v_sub_u32_e32 v4, 0, v1
	v_mul_lo_u32 v4, v4, v3
	v_mul_hi_u32 v4, v3, v4
	v_add_u32_e32 v3, v3, v4
	v_mul_hi_u32 v3, v2, v3
	v_mul_lo_u32 v4, v3, v1
	v_sub_u32_e32 v2, v2, v4
	v_add_u32_e32 v6, 1, v3
	v_cmp_ge_u32_e32 vcc, v2, v1
	v_sub_u32_e32 v4, v2, v1
	s_nop 0
	v_cndmask_b32_e32 v3, v3, v6, vcc
	v_cndmask_b32_e32 v2, v2, v4, vcc
	v_add_u32_e32 v4, 1, v3
	v_cmp_ge_u32_e32 vcc, v2, v1
	s_nop 1
	v_cndmask_b32_e32 v4, v3, v4, vcc
	v_mul_lo_u32 v2, v1, v4
	v_add_u32_e32 v1, v2, v1
	v_cmp_ne_u32_e32 vcc, v5, v1
	v_mov_b64_e32 v[2:3], s[10:11]
	s_and_saveexec_b64 s[8:9], vcc
	s_cbranch_execz .LBB0_98
	v_mov_b32_e32 v4, v1
	v_mov_b32_e32 v1, 0
	global_load_dword v2, v1, s[10:11] offset:-256 sc1
	s_mov_b64 s[24:25], 0
	s_waitcnt vmcnt(0)
	v_cmp_lt_u32_e32 vcc, v2, v4
	s_and_saveexec_b64 s[22:23], vcc
	s_cbranch_execz .LBB0_97
	s_add_u32 s20, s40, 0x8200
	s_addc_u32 s21, s41, 0
	s_mov_b32 s38, 1
	s_branch .LBB0_90

.LBB0_92:
	global_load_dword v2, v1, s[10:11] offset:-256 sc1
	s_add_i32 s38, s38, 1
	s_mov_b64 s[28:29], -1
	s_waitcnt vmcnt(0)
	v_cmp_ge_u32_e32 vcc, v2, v4
	s_orn2_b64 s[34:35], vcc, exec
	s_branch .LBB0_89

.LBB0_267:
	s_or_b64 exec, exec, s[10:11]
	v_cvt_f32_u32_e32 v5, v3
	s_waitcnt vmcnt(0)
	v_readfirstlane_b32 s8, v4
	v_sub_u32_e32 v4, 0, v3
	v_rcp_iflag_f32_e32 v5, v5
	v_add_u32_e32 v6, s8, v2
	v_mul_f32_e32 v5, 0x4f7ffffe, v5
	v_cvt_u32_f32_e32 v5, v5
	v_mul_lo_u32 v2, v4, v5
	v_mul_hi_u32 v2, v5, v2
	v_add_u32_e32 v2, v5, v2
	v_mul_hi_u32 v2, v6, v2
	v_mul_lo_u32 v4, v2, v3
	v_sub_u32_e32 v4, v6, v4
	v_add_u32_e32 v5, 1, v2
	v_cmp_ge_u32_e32 vcc, v4, v3
	s_nop 1
	v_cndmask_b32_e32 v2, v2, v5, vcc
	v_sub_u32_e32 v5, v4, v3
	v_cndmask_b32_e32 v4, v4, v5, vcc
	v_add_u32_e32 v5, 1, v2
	v_cmp_ge_u32_e32 vcc, v4, v3
	v_add_u32_e32 v4, 1, v6
	s_nop 0
	v_cndmask_b32_e32 v2, v2, v5, vcc
	v_mul_lo_u32 v5, v3, v2
	v_add_u32_e32 v3, v5, v3
	v_cmp_ne_u32_e32 vcc, v4, v3
	s_and_saveexec_b64 s[8:9], vcc
	s_xor_b64 s[8:9], exec, s[8:9]
	s_cbranch_execz .LBB0_281
	s_waitcnt lgkmcnt(0)
	v_mad_u32_u24 v2, v1, v2, v1
	buffer_inv sc1
	v_mov_b32_e32 v1, 0xb000
	global_load_dword v1, v1, s[40:41] offset:1024 sc1
	s_add_u32 s14, s40, 0xb400
	s_addc_u32 s15, s41, 0
	s_waitcnt vmcnt(0)
	v_cmp_lt_u32_e32 vcc, v1, v2
	s_and_saveexec_b64 s[10:11], vcc
	s_cbranch_execz .LBB0_280
	s_add_u32 s12, s40, 0x8200
	s_addc_u32 s13, s41, 0
	s_mov_b32 s26, 1
	s_mov_b64 s[16:17], 0
	v_mov_b32_e32 v1, 0
	s_branch .LBB0_271

.LBB0_273:
	global_load_dword v3, v1, s[14:15] sc1
	s_add_i32 s26, s26, 1
	s_mov_b64 s[22:23], -1
	s_waitcnt vmcnt(0)
	v_cmp_ge_u32_e32 vcc, v3, v2
	s_orn2_b64 s[20:21], vcc, exec
	s_branch .LBB0_270

.LBB0_284:
	s_or_b64 exec, exec, s[10:11]
	v_cvt_f32_u32_e32 v4, v1
	s_waitcnt vmcnt(0)
	v_readfirstlane_b32 s8, v3
	s_add_u32 s10, s40, 0xb500
	s_addc_u32 s11, s41, 0
	v_rcp_iflag_f32_e32 v4, v4
	v_add_u32_e32 v2, s8, v2
	v_add_u32_e32 v5, 1, v2
	s_mov_b64 s[12:13], -1
	v_mul_f32_e32 v3, 0x4f7ffffe, v4
	v_cvt_u32_f32_e32 v3, v3
	v_sub_u32_e32 v4, 0, v1
	v_mul_lo_u32 v4, v4, v3
	v_mul_hi_u32 v4, v3, v4
	v_add_u32_e32 v3, v3, v4
	v_mul_hi_u32 v3, v2, v3
	v_mul_lo_u32 v4, v3, v1
	v_sub_u32_e32 v2, v2, v4
	v_add_u32_e32 v6, 1, v3
	v_cmp_ge_u32_e32 vcc, v2, v1
	v_sub_u32_e32 v4, v2, v1
	s_nop 0
	v_cndmask_b32_e32 v3, v3, v6, vcc
	v_cndmask_b32_e32 v2, v2, v4, vcc
	v_add_u32_e32 v4, 1, v3
	v_cmp_ge_u32_e32 vcc, v2, v1
	s_nop 1
	v_cndmask_b32_e32 v4, v3, v4, vcc
	v_mul_lo_u32 v2, v1, v4
	v_add_u32_e32 v1, v2, v1
	v_cmp_ne_u32_e32 vcc, v5, v1
	v_mov_b64_e32 v[2:3], s[10:11]
	s_and_saveexec_b64 s[8:9], vcc
	s_cbranch_execz .LBB0_296
	v_mov_b32_e32 v4, v1
	v_mov_b32_e32 v1, 0
	global_load_dword v2, v1, s[10:11] offset:-256 sc1
	s_mov_b64 s[16:17], 0
	s_waitcnt vmcnt(0)
	v_cmp_lt_u32_e32 vcc, v2, v4
	s_and_saveexec_b64 s[14:15], vcc
	s_cbranch_execz .LBB0_295
	s_add_u32 s12, s40, 0x8200
	s_addc_u32 s13, s41, 0
	s_mov_b32 s26, 1
	s_branch .LBB0_288

.LBB0_290:
	global_load_dword v2, v1, s[10:11] offset:-256 sc1
	s_add_i32 s26, s26, 1
	s_mov_b64 s[20:21], -1
	s_waitcnt vmcnt(0)
	v_cmp_ge_u32_e32 vcc, v2, v4
	s_orn2_b64 s[24:25], vcc, exec
	s_branch .LBB0_287

.LBB0_3506:
	s_or_b64 exec, exec, s[10:11]
	v_cvt_f32_u32_e32 v5, v3
	s_waitcnt vmcnt(0)
	v_readfirstlane_b32 s3, v4
	v_sub_u32_e32 v4, 0, v3
	v_rcp_iflag_f32_e32 v5, v5
	v_add_u32_e32 v6, s3, v2
	v_mul_f32_e32 v5, 0x4f7ffffe, v5
	v_cvt_u32_f32_e32 v5, v5
	v_mul_lo_u32 v2, v4, v5
	v_mul_hi_u32 v2, v5, v2
	v_add_u32_e32 v2, v5, v2
	v_mul_hi_u32 v2, v6, v2
	v_mul_lo_u32 v4, v2, v3
	v_sub_u32_e32 v4, v6, v4
	v_add_u32_e32 v5, 1, v2
	v_cmp_ge_u32_e32 vcc, v4, v3
	s_nop 1
	v_cndmask_b32_e32 v2, v2, v5, vcc
	v_sub_u32_e32 v5, v4, v3
	v_cndmask_b32_e32 v4, v4, v5, vcc
	v_add_u32_e32 v5, 1, v2
	v_cmp_ge_u32_e32 vcc, v4, v3
	v_add_u32_e32 v4, 1, v6
	s_nop 0
	v_cndmask_b32_e32 v2, v2, v5, vcc
	v_mul_lo_u32 v5, v3, v2
	v_add_u32_e32 v3, v5, v3
	v_cmp_ne_u32_e32 vcc, v4, v3
	s_and_saveexec_b64 s[8:9], vcc
	s_xor_b64 s[8:9], exec, s[8:9]
	s_cbranch_execz .LBB0_3520
	s_waitcnt lgkmcnt(0)
	v_mad_u32_u24 v2, v1, v2, v1
	buffer_inv sc1
	v_mov_b32_e32 v1, 0xb000
	global_load_dword v1, v1, s[40:41] offset:1024 sc1
	s_add_u32 s14, s40, 0xb400
	s_addc_u32 s15, s41, 0
	s_waitcnt vmcnt(0)
	v_cmp_lt_u32_e32 vcc, v1, v2
	s_and_saveexec_b64 s[10:11], vcc
	s_cbranch_execz .LBB0_3519
	s_add_u32 s12, s40, 0x8200
	s_addc_u32 s13, s41, 0
	s_mov_b32 s3, 1
	s_mov_b64 s[16:17], 0
	v_mov_b32_e32 v1, 0
	s_branch .LBB0_3510

.LBB0_3512:
	global_load_dword v3, v1, s[14:15] sc1
	s_add_i32 s3, s3, 1
	s_mov_b64 s[22:23], -1
	s_waitcnt vmcnt(0)
	v_cmp_ge_u32_e32 vcc, v3, v2
	s_orn2_b64 s[20:21], vcc, exec
	s_branch .LBB0_3509

.LBB0_3523:
	s_or_b64 exec, exec, s[10:11]
	v_cvt_f32_u32_e32 v4, v1
	s_waitcnt vmcnt(0)
	v_readfirstlane_b32 s3, v3
	s_add_u32 s10, s40, 0xb500
	s_addc_u32 s11, s41, 0
	v_rcp_iflag_f32_e32 v4, v4
	v_add_u32_e32 v2, s3, v2
	v_add_u32_e32 v5, 1, v2
	s_mov_b64 s[12:13], -1
	v_mul_f32_e32 v3, 0x4f7ffffe, v4
	v_cvt_u32_f32_e32 v3, v3
	v_sub_u32_e32 v4, 0, v1
	v_mul_lo_u32 v4, v4, v3
	v_mul_hi_u32 v4, v3, v4
	v_add_u32_e32 v3, v3, v4
	v_mul_hi_u32 v3, v2, v3
	v_mul_lo_u32 v4, v3, v1
	v_sub_u32_e32 v2, v2, v4
	v_add_u32_e32 v6, 1, v3
	v_cmp_ge_u32_e32 vcc, v2, v1
	v_sub_u32_e32 v4, v2, v1
	s_nop 0
	v_cndmask_b32_e32 v3, v3, v6, vcc
	v_cndmask_b32_e32 v2, v2, v4, vcc
	v_add_u32_e32 v4, 1, v3
	v_cmp_ge_u32_e32 vcc, v2, v1
	s_nop 1
	v_cndmask_b32_e32 v4, v3, v4, vcc
	v_mul_lo_u32 v2, v1, v4
	v_add_u32_e32 v1, v2, v1
	v_cmp_ne_u32_e32 vcc, v5, v1
	v_mov_b64_e32 v[2:3], s[10:11]
	s_and_saveexec_b64 s[8:9], vcc
	s_cbranch_execz .LBB0_3535
	v_mov_b32_e32 v4, v1
	v_mov_b32_e32 v1, 0
	global_load_dword v2, v1, s[10:11] offset:-256 sc1
	s_mov_b64 s[16:17], 0
	s_waitcnt vmcnt(0)
	v_cmp_lt_u32_e32 vcc, v2, v4
	s_and_saveexec_b64 s[14:15], vcc
	s_cbranch_execz .LBB0_3534
	s_add_u32 s12, s40, 0x8200
	s_addc_u32 s13, s41, 0
	s_mov_b32 s3, 1
	s_branch .LBB0_3527

.LBB0_3529:
	global_load_dword v2, v1, s[10:11] offset:-256 sc1
	s_add_i32 s3, s3, 1
	s_mov_b64 s[20:21], -1
	s_waitcnt vmcnt(0)
	v_cmp_ge_u32_e32 vcc, v2, v4
	s_orn2_b64 s[24:25], vcc, exec
	s_branch .LBB0_3526
